# Fourier stage C: the eight B-fragment loads of a loop trip issued together at its top (free registers, MFMA operands renamed) instead of two dependent batches
# baseline (speedup 1.0000x reference)
.LBB0_493:
	s_waitcnt vmcnt(25)
	v_add_u32_e32 v88, v71, v74
	s_waitcnt vmcnt(24)
	v_add_u32_e32 v92, 16, v88
	v_ashrrev_i32_e32 v89, 31, v88
	v_ashrrev_i32_e32 v93, 31, v92
	v_lshlrev_b64 v[68:69], 8, v[88:89]
	v_lshlrev_b64 v[92:93], 8, v[92:93]
	v_lshl_add_u64 v[68:69], v[66:67], 0, v[68:69]
	v_lshl_add_u64 v[120:121], v[66:67], 0, v[92:93]
	global_load_dwordx4 v[188:191], v[68:69], off
	global_load_dwordx4 v[192:195], v[68:69], off offset:64
	global_load_dwordx4 v[196:199], v[120:121], off
	global_load_dwordx4 v[200:203], v[120:121], off offset:64
	global_load_dwordx4 v[204:207], v[68:69], off offset:128
	global_load_dwordx4 v[208:211], v[68:69], off offset:192
	global_load_dwordx4 v[212:215], v[120:121], off offset:128
	global_load_dwordx4 v[216:219], v[120:121], off offset:192
	v_bfe_u32 v75, v70, 5, 7
	v_and_b32_e32 v112, 0xffffe000, v73
	v_or3_b32 v116, v75, v112, v72
	v_and_b32_e32 v64, 0x180, v74
	v_and_or_b32 v117, v74, s16, v71
	v_lshlrev_b32_e32 v64, 1, v64
	v_lshl_add_u64 v[118:119], s[8:9], 0, v[64:65]
	v_lshlrev_b32_e32 v64, 1, v117
	v_ashrrev_i32_e32 v117, 31, v116
	v_or_b32_e32 v122, 0x80, v116
	v_or_b32_e32 v124, 0x100, v116
	v_or_b32_e32 v126, 0x180, v116
	v_or_b32_e32 v128, 0x800, v116
	v_or_b32_e32 v130, 0x880, v116
	v_or_b32_e32 v132, 0x900, v116
	v_or_b32_e32 v134, 0x980, v116
	v_or_b32_e32 v136, 0x1000, v116
	v_or_b32_e32 v138, 0x1080, v116
	v_or_b32_e32 v140, 0x1100, v116
	v_or_b32_e32 v142, 0x1180, v116
	v_or_b32_e32 v144, 0x1800, v116
	v_or_b32_e32 v146, 0x1880, v116
	v_or_b32_e32 v148, 0x1900, v116
	v_or_b32_e32 v150, 0x1980, v116
	v_lshl_add_u64 v[152:153], v[118:119], 0, v[64:65]
	v_lshlrev_b64 v[154:155], 11, v[116:117]
	v_add_u32_e32 v70, s20, v70
	v_ashrrev_i32_e32 v123, 31, v122
	v_ashrrev_i32_e32 v125, 31, v124
	v_ashrrev_i32_e32 v127, 31, v126
	v_ashrrev_i32_e32 v129, 31, v128
	v_ashrrev_i32_e32 v131, 31, v130
	v_ashrrev_i32_e32 v133, 31, v132
	v_ashrrev_i32_e32 v135, 31, v134
	v_ashrrev_i32_e32 v137, 31, v136
	v_ashrrev_i32_e32 v139, 31, v138
	v_ashrrev_i32_e32 v141, 31, v140
	v_ashrrev_i32_e32 v143, 31, v142
	v_ashrrev_i32_e32 v145, 31, v144
	v_ashrrev_i32_e32 v147, 31, v146
	v_ashrrev_i32_e32 v149, 31, v148
	v_ashrrev_i32_e32 v151, 31, v150
	v_cmp_lt_i32_e32 vcc, s17, v70
	v_add_u32_e32 v73, s12, v73
	v_add_u32_e32 v74, s13, v74
	s_or_b64 s[10:11], vcc, s[10:11]
	s_waitcnt vmcnt(7)
	v_mfma_f32_16x16x32_bf16 v[84:87], v[8:11], v[188:191], 0
	v_mfma_f32_16x16x32_bf16 v[88:91], v[16:19], v[188:191], 0
	v_mfma_f32_16x16x32_bf16 v[92:95], v[32:35], v[188:191], 0
	v_mfma_f32_16x16x32_bf16 v[76:79], v[48:51], v[188:191], 0
	s_waitcnt vmcnt(5)
	v_mfma_f32_16x16x32_bf16 v[104:107], v[8:11], v[196:199], 0
	v_mfma_f32_16x16x32_bf16 v[108:111], v[16:19], v[196:199], 0
	v_mfma_f32_16x16x32_bf16 v[112:115], v[32:35], v[196:199], 0
	v_mfma_f32_16x16x32_bf16 v[96:99], v[48:51], v[196:199], 0
	v_mfma_f32_16x16x32_bf16 v[84:87], v[0:3], v[192:195], v[84:87]
	v_mfma_f32_16x16x32_bf16 v[88:91], v[20:23], v[192:195], v[88:91]
	v_mfma_f32_16x16x32_bf16 v[92:95], v[36:39], v[192:195], v[92:95]
	v_mfma_f32_16x16x32_bf16 v[76:79], v[52:55], v[192:195], v[76:79]
	s_waitcnt vmcnt(4)
	v_mfma_f32_16x16x32_bf16 v[80:83], v[0:3], v[200:203], v[104:107]
	v_mfma_f32_16x16x32_bf16 v[104:107], v[20:23], v[200:203], v[108:111]
	v_mfma_f32_16x16x32_bf16 v[108:111], v[36:39], v[200:203], v[112:115]
	v_mfma_f32_16x16x32_bf16 v[96:99], v[52:55], v[200:203], v[96:99]
	s_nop 0
	s_nop 0
	s_nop 0
	s_nop 0
	v_lshl_add_u64 v[68:69], v[152:153], 0, v[154:155]
	s_waitcnt vmcnt(3)
	v_mfma_f32_16x16x32_bf16 v[84:87], v[4:7], v[204:207], v[84:87]
	v_mfma_f32_16x16x32_bf16 v[88:91], v[24:27], v[204:207], v[88:91]
	v_mfma_f32_16x16x32_bf16 v[92:95], v[40:43], v[204:207], v[92:95]
	v_mfma_f32_16x16x32_bf16 v[76:79], v[56:59], v[204:207], v[76:79]
	s_nop 0
	v_lshlrev_b64 v[120:121], 11, v[122:123]
	v_lshlrev_b64 v[122:123], 11, v[124:125]
	s_waitcnt vmcnt(1)
	v_mfma_f32_16x16x32_bf16 v[80:83], v[4:7], v[212:215], v[80:83]
	v_lshlrev_b64 v[124:125], 11, v[126:127]
	v_lshlrev_b64 v[126:127], 11, v[128:129]
	v_lshlrev_b64 v[128:129], 11, v[130:131]
	v_mfma_f32_16x16x32_bf16 v[104:107], v[24:27], v[212:215], v[104:107]
	v_lshlrev_b64 v[130:131], 11, v[132:133]
	v_lshlrev_b64 v[132:133], 11, v[138:139]
	v_lshlrev_b64 v[138:139], 11, v[144:145]
	v_mfma_f32_16x16x32_bf16 v[108:111], v[40:43], v[212:215], v[108:111]
	v_lshlrev_b64 v[144:145], 11, v[150:151]
	v_lshl_add_u64 v[120:121], v[152:153], 0, v[120:121]
	v_lshl_add_u64 v[122:123], v[152:153], 0, v[122:123]
	v_mfma_f32_16x16x32_bf16 v[96:99], v[56:59], v[212:215], v[96:99]
	v_lshlrev_b64 v[116:117], 11, v[134:135]
	v_lshlrev_b64 v[118:119], 11, v[136:137]
	v_lshlrev_b64 v[134:135], 11, v[140:141]
	v_mfma_f32_16x16x32_bf16 v[84:87], v[12:15], v[208:211], v[84:87]
	v_lshlrev_b64 v[136:137], 11, v[142:143]
	v_lshlrev_b64 v[140:141], 11, v[146:147]
	v_lshlrev_b64 v[142:143], 11, v[148:149]
	v_mfma_f32_16x16x32_bf16 v[88:91], v[28:31], v[208:211], v[88:91]
	v_lshl_add_u64 v[124:125], v[152:153], 0, v[124:125]
	s_nop 2
	v_cvt_pk_bf16_f32 v64, v84, s0
	v_lshl_add_u64 v[116:117], v[152:153], 0, v[116:117]
	v_mfma_f32_16x16x32_bf16 v[92:95], v[44:47], v[208:211], v[92:95]
	v_lshl_add_u64 v[118:119], v[152:153], 0, v[118:119]
	v_cvt_pk_bf16_f32 v75, v85, s0
	v_cvt_pk_bf16_f32 v84, v86, s0
	v_mfma_f32_16x16x32_bf16 v[76:79], v[60:63], v[208:211], v[76:79]
	v_lshl_add_u64 v[112:113], v[152:153], 0, v[126:127]
	v_lshl_add_u64 v[114:115], v[152:153], 0, v[128:129]
	v_lshl_add_u64 v[126:127], v[152:153], 0, v[130:131]
	s_waitcnt vmcnt(0)
	v_mfma_f32_16x16x32_bf16 v[80:83], v[12:15], v[216:219], v[80:83]
	v_lshl_add_u64 v[128:129], v[152:153], 0, v[132:133]
	v_lshl_add_u64 v[130:131], v[152:153], 0, v[134:135]
	v_lshl_add_u64 v[132:133], v[152:153], 0, v[136:137]
	v_mfma_f32_16x16x32_bf16 v[104:107], v[28:31], v[216:219], v[104:107]
	v_lshl_add_u64 v[134:135], v[152:153], 0, v[138:139]
	v_lshl_add_u64 v[136:137], v[152:153], 0, v[140:141]
	v_lshl_add_u64 v[138:139], v[152:153], 0, v[142:143]
	v_mfma_f32_16x16x32_bf16 v[108:111], v[44:47], v[216:219], v[108:111]
	v_lshl_add_u64 v[140:141], v[152:153], 0, v[144:145]
	v_cvt_pk_bf16_f32 v85, v87, s0
	v_cvt_pk_bf16_f32 v86, v88, s0
	v_mfma_f32_16x16x32_bf16 v[96:99], v[60:63], v[216:219], v[96:99]
	v_cvt_pk_bf16_f32 v87, v89, s0
	v_cvt_pk_bf16_f32 v88, v90, s0
	v_cvt_pk_bf16_f32 v89, v91, s0
	v_cvt_pk_bf16_f32 v90, v92, s0
	v_cvt_pk_bf16_f32 v91, v93, s0
	v_cvt_pk_bf16_f32 v92, v94, s0
	v_cvt_pk_bf16_f32 v93, v95, s0
	v_cvt_pk_bf16_f32 v76, v76, s0
	v_cvt_pk_bf16_f32 v77, v77, s0
	v_cvt_pk_bf16_f32 v78, v78, s0
	v_cvt_pk_bf16_f32 v79, v79, s0
	global_store_short v[68:69], v64, off
	global_store_short v[120:121], v75, off
	global_store_short v[122:123], v84, off
	global_store_short v[124:125], v85, off
	global_store_short v[112:113], v86, off
	global_store_short v[114:115], v87, off
	global_store_short v[126:127], v88, off
	global_store_short v[116:117], v89, off
	global_store_short v[118:119], v90, off
	global_store_short v[128:129], v91, off
	global_store_short v[130:131], v92, off
	global_store_short v[132:133], v93, off
	global_store_short v[134:135], v76, off
	global_store_short v[136:137], v77, off
	global_store_short v[138:139], v78, off
	global_store_short v[140:141], v79, off
	v_cvt_pk_bf16_f32 v64, v80, s0
	v_cvt_pk_bf16_f32 v75, v81, s0
	v_cvt_pk_bf16_f32 v76, v82, s0
	v_cvt_pk_bf16_f32 v77, v83, s0
	v_cvt_pk_bf16_f32 v78, v104, s0
	v_cvt_pk_bf16_f32 v79, v105, s0
	v_cvt_pk_bf16_f32 v80, v106, s0
	v_cvt_pk_bf16_f32 v81, v107, s0
	v_cvt_pk_bf16_f32 v82, v108, s0
	v_cvt_pk_bf16_f32 v83, v109, s0
	v_cvt_pk_bf16_f32 v84, v110, s0
	v_cvt_pk_bf16_f32 v85, v111, s0
	v_cvt_pk_bf16_f32 v86, v96, s0
	v_cvt_pk_bf16_f32 v87, v97, s0
	v_cvt_pk_bf16_f32 v88, v98, s0
	v_cvt_pk_bf16_f32 v89, v99, s0
	global_store_short v[68:69], v64, off offset:32
	global_store_short v[120:121], v75, off offset:32
	global_store_short v[122:123], v76, off offset:32
	global_store_short v[124:125], v77, off offset:32
	global_store_short v[112:113], v78, off offset:32
	global_store_short v[114:115], v79, off offset:32
	global_store_short v[126:127], v80, off offset:32
	global_store_short v[116:117], v81, off offset:32
	global_store_short v[118:119], v82, off offset:32
	global_store_short v[128:129], v83, off offset:32
	global_store_short v[130:131], v84, off offset:32
	global_store_short v[132:133], v85, off offset:32
	global_store_short v[134:135], v86, off offset:32
	global_store_short v[136:137], v87, off offset:32
	global_store_short v[138:139], v88, off offset:32
	global_store_short v[140:141], v89, off offset:32
	s_andn2_b64 exec, exec, s[10:11]
	s_cbranch_execnz .LBB0_493
